# v11 + 8 more expert weight mats converted by WGs>=128 at the end of the ev_in phases (they run one ev_sw unit fewer): windows E0=4 U1=8 E2=4 U3=8 mats
# baseline (speedup 1.0000x reference)
.LBB0_654:
	s_barrier
	v_readlane_b32 s46, v255, 4
	s_sub_i32 s42, s88, 0x80
	s_lshl_b32 s42, s42, 3
	s_lshr_b32 s5, s33, 6
	s_add_i32 s42, s42, s5
	s_mul_i32 s5, s5, 0x4200
	s_movk_i32 s45, 120
	s_movk_i32 s4, 8
	s_movk_i32 vcc_lo, 108
	s_movk_i32 vcc_hi, 8
	s_cmp_eq_u32 s46, 1
	s_cselect_b32 s45, vcc_lo, s45
	s_cselect_b32 s4, vcc_hi, s4
	s_lshl_b32 s44, s4, 9
	s_mul_i32 s43, s4, 0x300
	v_readlane_b32 s8, v252, 0
	v_readlane_b32 s9, v252, 1
	v_mbcnt_lo_u32_b32 v13, -1, 0
	v_mbcnt_hi_u32_b32 v13, -1, v13
	s_load_dwordx2 s[6:7], s[8:9], 0xa0
	s_load_dwordx2 s[10:11], s[8:9], 0xd8
	s_load_dwordx2 s[8:9], s[8:9], 0xb0
	s_movk_i32 s46, 0x84
	s_movk_i32 s47, 0x840
	v_and_b32_e32 v14, 31, v13
	v_lshlrev_b32_e32 v14, 2, v14
	v_lshrrev_b32_e32 v15, 5, v13
	v_mov_b32_e32 v4, s5
	v_mad_u32_u24 v4, v15, s46, v4
	v_add_u32_e32 v4, v4, v14
	v_and_b32_e32 v10, 7, v13
	v_lshrrev_b32_e32 v11, 3, v13
	v_mov_b32_e32 v5, s5
	v_mad_u32_u24 v5, v10, s47, v5
	v_lshl_add_u32 v5, v11, 2, v5
	v_lshlrev_b32_e32 v6, 10, v11
	v_lshl_add_u32 v6, v10, 4, v6
	v_add_u32_e32 v7, 0x2000, v6
	v_add_u32_e32 v8, 0x4000, v6
	v_add_u32_e32 v9, 0x6000, v6
	s_waitcnt lgkmcnt(0)
	s_cmp_lt_u32 s42, s43
	s_cbranch_scc0 .LcvU_done
	s_cmp_lt_u32 s42, s44
	s_cbranch_scc0 .LcvU_dn0
	s_lshr_b32 s4, s42, 9
	s_add_i32 s4, s4, s45
	s_bfe_u32 s5, s42, 0x30006
	s_and_b32 vcc_lo, s42, 63
	s_lshl_b32 s46, s4, 23
	s_lshl_b32 s47, s5, 20
	s_add_u32 s46, s46, s47
	s_lshl_b32 s47, vcc_lo, 7
	s_add_u32 s46, s46, s47
	s_add_u32 s46, s46, s6
	s_addc_u32 s47, s7, 0
	s_lshl_b32 s52, s4, 21
	s_add_u32 s52, s52, 0x4400000
	s_lshl_b32 s53, s5, 7
	s_add_u32 s52, s52, s53
	s_bfe_u32 s53, vcc_lo, 0x30002
	s_lshl_b32 s53, s53, 18
	s_add_u32 s52, s52, s53
	s_lshr_b32 s53, vcc_lo, 5
	s_lshl_b32 s53, s53, 17
	s_add_u32 s52, s52, s53
	s_and_b32 s53, vcc_lo, 3
	s_lshl_b32 s53, s53, 15
	s_add_u32 s52, s52, s53
	s_add_u32 s52, s52, s10
	s_addc_u32 s53, s11, 0
	s_mov_b32 s51, 0x42000000
	s_movk_i32 s5, 0x2000
	s_movk_i32 s4, 0x4000
	s_branch .LcvU_ld0

.LBB0_1090:
	s_barrier
	s_cmpk_lt_u32 s88, 0x80
	s_cbranch_scc1 .LcvE_done
	v_readlane_b32 s38, v255, 4
	s_sub_i32 s64, s88, 0x80
	s_lshl_b32 s64, s64, 3
	s_lshr_b32 s5, s33, 6
	s_add_i32 s64, s64, s5
	s_mul_i32 s5, s5, 0x4200
	s_movk_i32 s67, 116
	s_movk_i32 s4, 4
	s_movk_i32 vcc_lo, 104
	s_movk_i32 vcc_hi, 4
	s_cmp_eq_u32 s38, 0
	s_cselect_b32 s67, vcc_lo, s67
	s_cselect_b32 s4, vcc_hi, s4
	s_lshl_b32 s66, s4, 9
	s_mul_i32 s65, s4, 0x300
	v_readlane_b32 s8, v252, 0
	v_readlane_b32 s9, v252, 1
	v_mbcnt_lo_u32_b32 v13, -1, 0
	v_mbcnt_hi_u32_b32 v13, -1, v13
	s_load_dwordx2 s[6:7], s[8:9], 0xa0
	s_load_dwordx2 s[10:11], s[8:9], 0xd8
	s_load_dwordx2 s[8:9], s[8:9], 0xb0
	s_movk_i32 s38, 0x84
	s_movk_i32 s39, 0x840
	v_and_b32_e32 v14, 31, v13
	v_lshlrev_b32_e32 v14, 2, v14
	v_lshrrev_b32_e32 v15, 5, v13
	v_mov_b32_e32 v4, s5
	v_mad_u32_u24 v4, v15, s38, v4
	v_add_u32_e32 v4, v4, v14
	v_and_b32_e32 v10, 7, v13
	v_lshrrev_b32_e32 v11, 3, v13
	v_mov_b32_e32 v5, s5
	v_mad_u32_u24 v5, v10, s39, v5
	v_lshl_add_u32 v5, v11, 2, v5
	v_lshlrev_b32_e32 v6, 10, v11
	v_lshl_add_u32 v6, v10, 4, v6
	v_add_u32_e32 v7, 0x2000, v6
	v_add_u32_e32 v8, 0x4000, v6
	v_add_u32_e32 v9, 0x6000, v6
	s_waitcnt lgkmcnt(0)
	s_cmp_lt_u32 s64, s65
	s_cbranch_scc0 .LcvE_done
	s_cmp_lt_u32 s64, s66
	s_cbranch_scc0 .LcvE_dn0
	s_lshr_b32 s4, s64, 9
	s_add_i32 s4, s4, s67
	s_bfe_u32 s5, s64, 0x30006
	s_and_b32 vcc_lo, s64, 63
	s_lshl_b32 s38, s4, 23
	s_lshl_b32 s39, s5, 20
	s_add_u32 s38, s38, s39
	s_lshl_b32 s39, vcc_lo, 7
	s_add_u32 s38, s38, s39
	s_add_u32 s38, s38, s6
	s_addc_u32 s39, s7, 0
	s_lshl_b32 s42, s4, 21
	s_add_u32 s42, s42, 0x4400000
	s_lshl_b32 s43, s5, 7
	s_add_u32 s42, s42, s43
	s_bfe_u32 s43, vcc_lo, 0x30002
	s_lshl_b32 s43, s43, 18
	s_add_u32 s42, s42, s43
	s_lshr_b32 s43, vcc_lo, 5
	s_lshl_b32 s43, s43, 17
	s_add_u32 s42, s42, s43
	s_and_b32 s43, vcc_lo, 3
	s_lshl_b32 s43, s43, 15
	s_add_u32 s42, s42, s43
	s_add_u32 s42, s42, s10
	s_addc_u32 s43, s11, 0
	s_mov_b32 s63, 0x42000000
	s_movk_i32 s5, 0x2000
	s_movk_i32 s4, 0x4000
	s_branch .LcvE_ld0
.LcvE_dn0:
	s_sub_u32 vcc_hi, s64, s66
	s_lshr_b32 s4, vcc_hi, 8
	s_add_i32 s4, s4, s67
	s_bfe_u32 s5, vcc_hi, 0x30005
	s_and_b32 vcc_lo, vcc_hi, 31
	s_lshl_b32 s38, s4, 22
	s_lshl_b32 s39, s5, 19
	s_add_u32 s38, s38, s39
	s_lshl_b32 s39, vcc_lo, 7
	s_add_u32 s38, s38, s39
	s_add_u32 s38, s38, s8
	s_addc_u32 s39, s9, 0
	s_lshl_b32 s42, s4, 20
	s_add_u32 s42, s42, 0x24400000
	s_lshl_b32 s43, s5, 7
	s_add_u32 s42, s42, s43
	s_lshl_b32 s43, vcc_lo, 15
	s_add_u32 s42, s42, s43
	s_add_u32 s42, s42, s10
	s_addc_u32 s43, s11, 0
	s_mov_b32 s63, 0x42800000
	s_movk_i32 s5, 0x1000
	s_movk_i32 s4, 0x2000
.LcvE_ld0:
	v_mad_u32_u24 v12, v15, s5, v14
	global_load_dword v64, v12, s[38:39]
	s_add_u32 s38, s38, s4
	s_addc_u32 s39, s39, 0
	global_load_dword v65, v12, s[38:39]
	s_add_u32 s38, s38, s4
	s_addc_u32 s39, s39, 0
	global_load_dword v66, v12, s[38:39]
	s_add_u32 s38, s38, s4
	s_addc_u32 s39, s39, 0
	global_load_dword v67, v12, s[38:39]
	s_add_u32 s38, s38, s4
	s_addc_u32 s39, s39, 0
	global_load_dword v68, v12, s[38:39]
	s_add_u32 s38, s38, s4
	s_addc_u32 s39, s39, 0
	global_load_dword v69, v12, s[38:39]
	s_add_u32 s38, s38, s4
	s_addc_u32 s39, s39, 0
	global_load_dword v70, v12, s[38:39]
	s_add_u32 s38, s38, s4
	s_addc_u32 s39, s39, 0
	global_load_dword v71, v12, s[38:39]
	s_add_u32 s38, s38, s4
	s_addc_u32 s39, s39, 0
	global_load_dword v72, v12, s[38:39]
	s_add_u32 s38, s38, s4
	s_addc_u32 s39, s39, 0
	global_load_dword v73, v12, s[38:39]
	s_add_u32 s38, s38, s4
	s_addc_u32 s39, s39, 0
	global_load_dword v74, v12, s[38:39]
	s_add_u32 s38, s38, s4
	s_addc_u32 s39, s39, 0
	global_load_dword v75, v12, s[38:39]
	s_add_u32 s38, s38, s4
	s_addc_u32 s39, s39, 0
	global_load_dword v76, v12, s[38:39]
	s_add_u32 s38, s38, s4
	s_addc_u32 s39, s39, 0
	global_load_dword v77, v12, s[38:39]
	s_add_u32 s38, s38, s4
	s_addc_u32 s39, s39, 0
	global_load_dword v78, v12, s[38:39]
	s_add_u32 s38, s38, s4
	s_addc_u32 s39, s39, 0
	global_load_dword v79, v12, s[38:39]
	s_add_u32 s38, s38, s4
	s_addc_u32 s39, s39, 0
	global_load_dword v80, v12, s[38:39]
	s_add_u32 s38, s38, s4
	s_addc_u32 s39, s39, 0
	global_load_dword v81, v12, s[38:39]
	s_add_u32 s38, s38, s4
	s_addc_u32 s39, s39, 0
	global_load_dword v82, v12, s[38:39]
	s_add_u32 s38, s38, s4
	s_addc_u32 s39, s39, 0
	global_load_dword v83, v12, s[38:39]
	s_add_u32 s38, s38, s4
	s_addc_u32 s39, s39, 0
	global_load_dword v84, v12, s[38:39]
	s_add_u32 s38, s38, s4
	s_addc_u32 s39, s39, 0
	global_load_dword v85, v12, s[38:39]
	s_add_u32 s38, s38, s4
	s_addc_u32 s39, s39, 0
	global_load_dword v86, v12, s[38:39]
	s_add_u32 s38, s38, s4
	s_addc_u32 s39, s39, 0
	global_load_dword v87, v12, s[38:39]
	s_add_u32 s38, s38, s4
	s_addc_u32 s39, s39, 0
	global_load_dword v88, v12, s[38:39]
	s_add_u32 s38, s38, s4
	s_addc_u32 s39, s39, 0
	global_load_dword v89, v12, s[38:39]
	s_add_u32 s38, s38, s4
	s_addc_u32 s39, s39, 0
	global_load_dword v90, v12, s[38:39]
	s_add_u32 s38, s38, s4
	s_addc_u32 s39, s39, 0
	global_load_dword v91, v12, s[38:39]
	s_add_u32 s38, s38, s4
	s_addc_u32 s39, s39, 0
	global_load_dword v92, v12, s[38:39]
	s_add_u32 s38, s38, s4
	s_addc_u32 s39, s39, 0
	global_load_dword v93, v12, s[38:39]
	s_add_u32 s38, s38, s4
	s_addc_u32 s39, s39, 0
	global_load_dword v94, v12, s[38:39]
	s_add_u32 s38, s38, s4
	s_addc_u32 s39, s39, 0
	global_load_dword v95, v12, s[38:39]
	s_add_u32 s38, s38, s4
	s_addc_u32 s39, s39, 0
	global_load_dword v96, v12, s[38:39]
	s_add_u32 s38, s38, s4
	s_addc_u32 s39, s39, 0
	global_load_dword v97, v12, s[38:39]
	s_add_u32 s38, s38, s4
	s_addc_u32 s39, s39, 0
	global_load_dword v98, v12, s[38:39]
	s_add_u32 s38, s38, s4
	s_addc_u32 s39, s39, 0
	global_load_dword v99, v12, s[38:39]
	s_add_u32 s38, s38, s4
	s_addc_u32 s39, s39, 0
	global_load_dword v100, v12, s[38:39]
	s_add_u32 s38, s38, s4
	s_addc_u32 s39, s39, 0
	global_load_dword v101, v12, s[38:39]
	s_add_u32 s38, s38, s4
	s_addc_u32 s39, s39, 0
	global_load_dword v102, v12, s[38:39]
	s_add_u32 s38, s38, s4
	s_addc_u32 s39, s39, 0
	global_load_dword v103, v12, s[38:39]
	s_add_u32 s38, s38, s4
	s_addc_u32 s39, s39, 0
	global_load_dword v104, v12, s[38:39]
	s_add_u32 s38, s38, s4
	s_addc_u32 s39, s39, 0
	global_load_dword v105, v12, s[38:39]
	s_add_u32 s38, s38, s4
	s_addc_u32 s39, s39, 0
	global_load_dword v106, v12, s[38:39]
	s_add_u32 s38, s38, s4
	s_addc_u32 s39, s39, 0
	global_load_dword v107, v12, s[38:39]
	s_add_u32 s38, s38, s4
	s_addc_u32 s39, s39, 0
	global_load_dword v108, v12, s[38:39]
	s_add_u32 s38, s38, s4
	s_addc_u32 s39, s39, 0
	global_load_dword v109, v12, s[38:39]
	s_add_u32 s38, s38, s4
	s_addc_u32 s39, s39, 0
	global_load_dword v110, v12, s[38:39]
	s_add_u32 s38, s38, s4
	s_addc_u32 s39, s39, 0
	global_load_dword v111, v12, s[38:39]
	s_add_u32 s38, s38, s4
	s_addc_u32 s39, s39, 0
	global_load_dword v112, v12, s[38:39]
	s_add_u32 s38, s38, s4
	s_addc_u32 s39, s39, 0
	global_load_dword v113, v12, s[38:39]
	s_add_u32 s38, s38, s4
	s_addc_u32 s39, s39, 0
	global_load_dword v114, v12, s[38:39]
	s_add_u32 s38, s38, s4
	s_addc_u32 s39, s39, 0
	global_load_dword v115, v12, s[38:39]
	s_add_u32 s38, s38, s4
	s_addc_u32 s39, s39, 0
	global_load_dword v116, v12, s[38:39]
	s_add_u32 s38, s38, s4
	s_addc_u32 s39, s39, 0
	global_load_dword v117, v12, s[38:39]
	s_add_u32 s38, s38, s4
	s_addc_u32 s39, s39, 0
	global_load_dword v118, v12, s[38:39]
	s_add_u32 s38, s38, s4
	s_addc_u32 s39, s39, 0
	global_load_dword v119, v12, s[38:39]
	s_add_u32 s38, s38, s4
	s_addc_u32 s39, s39, 0
	global_load_dword v120, v12, s[38:39]
	s_add_u32 s38, s38, s4
	s_addc_u32 s39, s39, 0
	global_load_dword v121, v12, s[38:39]
	s_add_u32 s38, s38, s4
	s_addc_u32 s39, s39, 0
	global_load_dword v122, v12, s[38:39]
	s_add_u32 s38, s38, s4
	s_addc_u32 s39, s39, 0
	global_load_dword v123, v12, s[38:39]
	s_add_u32 s38, s38, s4
	s_addc_u32 s39, s39, 0
	global_load_dword v124, v12, s[38:39]
	s_add_u32 s38, s38, s4
	s_addc_u32 s39, s39, 0
	global_load_dword v125, v12, s[38:39]
	s_add_u32 s38, s38, s4
	s_addc_u32 s39, s39, 0
	global_load_dword v126, v12, s[38:39]
	s_add_u32 s38, s38, s4
	s_addc_u32 s39, s39, 0
	global_load_dword v127, v12, s[38:39]
	s_waitcnt vmcnt(0)
	s_branch .LcvE_body

.LcvE_body:
	s_mov_b64 s[40:41], s[42:43]
	s_mov_b32 s46, s63
	ds_write_b32 v4, v64
	ds_write_b32 v4, v65 offset:264
	ds_write_b32 v4, v66 offset:528
	ds_write_b32 v4, v67 offset:792
	ds_write_b32 v4, v68 offset:1056
	ds_write_b32 v4, v69 offset:1320
	ds_write_b32 v4, v70 offset:1584
	ds_write_b32 v4, v71 offset:1848
	ds_write_b32 v4, v72 offset:2112
	ds_write_b32 v4, v73 offset:2376
	ds_write_b32 v4, v74 offset:2640
	ds_write_b32 v4, v75 offset:2904
	ds_write_b32 v4, v76 offset:3168
	ds_write_b32 v4, v77 offset:3432
	ds_write_b32 v4, v78 offset:3696
	ds_write_b32 v4, v79 offset:3960
	ds_write_b32 v4, v80 offset:4224
	ds_write_b32 v4, v81 offset:4488
	ds_write_b32 v4, v82 offset:4752
	ds_write_b32 v4, v83 offset:5016
	ds_write_b32 v4, v84 offset:5280
	ds_write_b32 v4, v85 offset:5544
	ds_write_b32 v4, v86 offset:5808
	ds_write_b32 v4, v87 offset:6072
	ds_write_b32 v4, v88 offset:6336
	ds_write_b32 v4, v89 offset:6600
	ds_write_b32 v4, v90 offset:6864
	ds_write_b32 v4, v91 offset:7128
	ds_write_b32 v4, v92 offset:7392
	ds_write_b32 v4, v93 offset:7656
	ds_write_b32 v4, v94 offset:7920
	ds_write_b32 v4, v95 offset:8184
	ds_write_b32 v4, v96 offset:8448
	ds_write_b32 v4, v97 offset:8712
	ds_write_b32 v4, v98 offset:8976
	ds_write_b32 v4, v99 offset:9240
	ds_write_b32 v4, v100 offset:9504
	ds_write_b32 v4, v101 offset:9768
	ds_write_b32 v4, v102 offset:10032
	ds_write_b32 v4, v103 offset:10296
	ds_write_b32 v4, v104 offset:10560
	ds_write_b32 v4, v105 offset:10824
	ds_write_b32 v4, v106 offset:11088
	ds_write_b32 v4, v107 offset:11352
	ds_write_b32 v4, v108 offset:11616
	ds_write_b32 v4, v109 offset:11880
	ds_write_b32 v4, v110 offset:12144
	ds_write_b32 v4, v111 offset:12408
	ds_write_b32 v4, v112 offset:12672
	ds_write_b32 v4, v113 offset:12936
	ds_write_b32 v4, v114 offset:13200
	ds_write_b32 v4, v115 offset:13464
	ds_write_b32 v4, v116 offset:13728
	ds_write_b32 v4, v117 offset:13992
	ds_write_b32 v4, v118 offset:14256
	ds_write_b32 v4, v119 offset:14520
	ds_write_b32 v4, v120 offset:14784
	ds_write_b32 v4, v121 offset:15048
	ds_write_b32 v4, v122 offset:15312
	ds_write_b32 v4, v123 offset:15576
	ds_write_b32 v4, v124 offset:15840
	ds_write_b32 v4, v125 offset:16104
	ds_write_b32 v4, v126 offset:16368
	ds_write_b32 v4, v127 offset:16632
	s_addk_i32 s64, 0x400
	s_cmp_lt_u32 s64, s65
	s_cbranch_scc0 .LcvE_nonext
	s_cmp_lt_u32 s64, s66
	s_cbranch_scc0 .LcvE_dn1
	s_lshr_b32 s4, s64, 9
	s_add_i32 s4, s4, s67
	s_bfe_u32 s5, s64, 0x30006
	s_and_b32 vcc_lo, s64, 63
	s_lshl_b32 s38, s4, 23
	s_lshl_b32 s39, s5, 20
	s_add_u32 s38, s38, s39
	s_lshl_b32 s39, vcc_lo, 7
	s_add_u32 s38, s38, s39
	s_add_u32 s38, s38, s6
	s_addc_u32 s39, s7, 0
	s_lshl_b32 s42, s4, 21
	s_add_u32 s42, s42, 0x4400000
	s_lshl_b32 s43, s5, 7
	s_add_u32 s42, s42, s43
	s_bfe_u32 s43, vcc_lo, 0x30002
	s_lshl_b32 s43, s43, 18
	s_add_u32 s42, s42, s43
	s_lshr_b32 s43, vcc_lo, 5
	s_lshl_b32 s43, s43, 17
	s_add_u32 s42, s42, s43
	s_and_b32 s43, vcc_lo, 3
	s_lshl_b32 s43, s43, 15
	s_add_u32 s42, s42, s43
	s_add_u32 s42, s42, s10
	s_addc_u32 s43, s11, 0
	s_mov_b32 s63, 0x42000000
	s_movk_i32 s5, 0x2000
	s_movk_i32 s4, 0x4000
	s_branch .LcvE_ld1

.LcvE_ld1:
	v_mad_u32_u24 v12, v15, s5, v14
	global_load_dword v64, v12, s[38:39]
	s_add_u32 s38, s38, s4
	s_addc_u32 s39, s39, 0
	global_load_dword v65, v12, s[38:39]
	s_add_u32 s38, s38, s4
	s_addc_u32 s39, s39, 0
	global_load_dword v66, v12, s[38:39]
	s_add_u32 s38, s38, s4
	s_addc_u32 s39, s39, 0
	global_load_dword v67, v12, s[38:39]
	s_add_u32 s38, s38, s4
	s_addc_u32 s39, s39, 0
	global_load_dword v68, v12, s[38:39]
	s_add_u32 s38, s38, s4
	s_addc_u32 s39, s39, 0
	global_load_dword v69, v12, s[38:39]
	s_add_u32 s38, s38, s4
	s_addc_u32 s39, s39, 0
	global_load_dword v70, v12, s[38:39]
	s_add_u32 s38, s38, s4
	s_addc_u32 s39, s39, 0
	global_load_dword v71, v12, s[38:39]
	s_add_u32 s38, s38, s4
	s_addc_u32 s39, s39, 0
	global_load_dword v72, v12, s[38:39]
	s_add_u32 s38, s38, s4
	s_addc_u32 s39, s39, 0
	global_load_dword v73, v12, s[38:39]
	s_add_u32 s38, s38, s4
	s_addc_u32 s39, s39, 0
	global_load_dword v74, v12, s[38:39]
	s_add_u32 s38, s38, s4
	s_addc_u32 s39, s39, 0
	global_load_dword v75, v12, s[38:39]
	s_add_u32 s38, s38, s4
	s_addc_u32 s39, s39, 0
	global_load_dword v76, v12, s[38:39]
	s_add_u32 s38, s38, s4
	s_addc_u32 s39, s39, 0
	global_load_dword v77, v12, s[38:39]
	s_add_u32 s38, s38, s4
	s_addc_u32 s39, s39, 0
	global_load_dword v78, v12, s[38:39]
	s_add_u32 s38, s38, s4
	s_addc_u32 s39, s39, 0
	global_load_dword v79, v12, s[38:39]
	s_add_u32 s38, s38, s4
	s_addc_u32 s39, s39, 0
	global_load_dword v80, v12, s[38:39]
	s_add_u32 s38, s38, s4
	s_addc_u32 s39, s39, 0
	global_load_dword v81, v12, s[38:39]
	s_add_u32 s38, s38, s4
	s_addc_u32 s39, s39, 0
	global_load_dword v82, v12, s[38:39]
	s_add_u32 s38, s38, s4
	s_addc_u32 s39, s39, 0
	global_load_dword v83, v12, s[38:39]
	s_add_u32 s38, s38, s4
	s_addc_u32 s39, s39, 0
	global_load_dword v84, v12, s[38:39]
	s_add_u32 s38, s38, s4
	s_addc_u32 s39, s39, 0
	global_load_dword v85, v12, s[38:39]
	s_add_u32 s38, s38, s4
	s_addc_u32 s39, s39, 0
	global_load_dword v86, v12, s[38:39]
	s_add_u32 s38, s38, s4
	s_addc_u32 s39, s39, 0
	global_load_dword v87, v12, s[38:39]
	s_add_u32 s38, s38, s4
	s_addc_u32 s39, s39, 0
	global_load_dword v88, v12, s[38:39]
	s_add_u32 s38, s38, s4
	s_addc_u32 s39, s39, 0
	global_load_dword v89, v12, s[38:39]
	s_add_u32 s38, s38, s4
	s_addc_u32 s39, s39, 0
	global_load_dword v90, v12, s[38:39]
	s_add_u32 s38, s38, s4
	s_addc_u32 s39, s39, 0
	global_load_dword v91, v12, s[38:39]
	s_add_u32 s38, s38, s4
	s_addc_u32 s39, s39, 0
	global_load_dword v92, v12, s[38:39]
	s_add_u32 s38, s38, s4
	s_addc_u32 s39, s39, 0
	global_load_dword v93, v12, s[38:39]
	s_add_u32 s38, s38, s4
	s_addc_u32 s39, s39, 0
	global_load_dword v94, v12, s[38:39]
	s_add_u32 s38, s38, s4
	s_addc_u32 s39, s39, 0
	global_load_dword v95, v12, s[38:39]
	s_add_u32 s38, s38, s4
	s_addc_u32 s39, s39, 0
	global_load_dword v96, v12, s[38:39]
	s_add_u32 s38, s38, s4
	s_addc_u32 s39, s39, 0
	global_load_dword v97, v12, s[38:39]
	s_add_u32 s38, s38, s4
	s_addc_u32 s39, s39, 0
	global_load_dword v98, v12, s[38:39]
	s_add_u32 s38, s38, s4
	s_addc_u32 s39, s39, 0
	global_load_dword v99, v12, s[38:39]
	s_add_u32 s38, s38, s4
	s_addc_u32 s39, s39, 0
	global_load_dword v100, v12, s[38:39]
	s_add_u32 s38, s38, s4
	s_addc_u32 s39, s39, 0
	global_load_dword v101, v12, s[38:39]
	s_add_u32 s38, s38, s4
	s_addc_u32 s39, s39, 0
	global_load_dword v102, v12, s[38:39]
	s_add_u32 s38, s38, s4
	s_addc_u32 s39, s39, 0
	global_load_dword v103, v12, s[38:39]
	s_add_u32 s38, s38, s4
	s_addc_u32 s39, s39, 0
	global_load_dword v104, v12, s[38:39]
	s_add_u32 s38, s38, s4
	s_addc_u32 s39, s39, 0
	global_load_dword v105, v12, s[38:39]
	s_add_u32 s38, s38, s4
	s_addc_u32 s39, s39, 0
	global_load_dword v106, v12, s[38:39]
	s_add_u32 s38, s38, s4
	s_addc_u32 s39, s39, 0
	global_load_dword v107, v12, s[38:39]
	s_add_u32 s38, s38, s4
	s_addc_u32 s39, s39, 0
	global_load_dword v108, v12, s[38:39]
	s_add_u32 s38, s38, s4
	s_addc_u32 s39, s39, 0
	global_load_dword v109, v12, s[38:39]
	s_add_u32 s38, s38, s4
	s_addc_u32 s39, s39, 0
	global_load_dword v110, v12, s[38:39]
	s_add_u32 s38, s38, s4
	s_addc_u32 s39, s39, 0
	global_load_dword v111, v12, s[38:39]
	s_add_u32 s38, s38, s4
	s_addc_u32 s39, s39, 0
	global_load_dword v112, v12, s[38:39]
	s_add_u32 s38, s38, s4
	s_addc_u32 s39, s39, 0
	global_load_dword v113, v12, s[38:39]
	s_add_u32 s38, s38, s4
	s_addc_u32 s39, s39, 0
	global_load_dword v114, v12, s[38:39]
	s_add_u32 s38, s38, s4
	s_addc_u32 s39, s39, 0
	global_load_dword v115, v12, s[38:39]
	s_add_u32 s38, s38, s4
	s_addc_u32 s39, s39, 0
	global_load_dword v116, v12, s[38:39]
	s_add_u32 s38, s38, s4
	s_addc_u32 s39, s39, 0
	global_load_dword v117, v12, s[38:39]
	s_add_u32 s38, s38, s4
	s_addc_u32 s39, s39, 0
	global_load_dword v118, v12, s[38:39]
	s_add_u32 s38, s38, s4
	s_addc_u32 s39, s39, 0
	global_load_dword v119, v12, s[38:39]
	s_add_u32 s38, s38, s4
	s_addc_u32 s39, s39, 0
	global_load_dword v120, v12, s[38:39]
	s_add_u32 s38, s38, s4
	s_addc_u32 s39, s39, 0
	global_load_dword v121, v12, s[38:39]
	s_add_u32 s38, s38, s4
	s_addc_u32 s39, s39, 0
	global_load_dword v122, v12, s[38:39]
	s_add_u32 s38, s38, s4
	s_addc_u32 s39, s39, 0
	global_load_dword v123, v12, s[38:39]
	s_add_u32 s38, s38, s4
	s_addc_u32 s39, s39, 0
	global_load_dword v124, v12, s[38:39]
	s_add_u32 s38, s38, s4
	s_addc_u32 s39, s39, 0
	global_load_dword v125, v12, s[38:39]
	s_add_u32 s38, s38, s4
	s_addc_u32 s39, s39, 0
	global_load_dword v126, v12, s[38:39]
	s_add_u32 s38, s38, s4
	s_addc_u32 s39, s39, 0
	global_load_dword v127, v12, s[38:39]
.LcvE_nonext:
	s_waitcnt lgkmcnt(0)
	ds_read_b32 v16, v5
	ds_read_b32 v17, v5 offset:132
	ds_read_b32 v18, v5 offset:264
	ds_read_b32 v19, v5 offset:396
	ds_read_b32 v20, v5 offset:528
	ds_read_b32 v21, v5 offset:660
	ds_read_b32 v22, v5 offset:792
	ds_read_b32 v23, v5 offset:924
	ds_read_b32 v24, v5 offset:1056
	ds_read_b32 v25, v5 offset:1188
	ds_read_b32 v26, v5 offset:1320
	ds_read_b32 v27, v5 offset:1452
	ds_read_b32 v28, v5 offset:1584
	ds_read_b32 v29, v5 offset:1716
	ds_read_b32 v30, v5 offset:1848
	ds_read_b32 v31, v5 offset:1980
	ds_read_b32 v32, v5 offset:32
	ds_read_b32 v33, v5 offset:164
	ds_read_b32 v34, v5 offset:296
	ds_read_b32 v35, v5 offset:428
	ds_read_b32 v36, v5 offset:560
	ds_read_b32 v37, v5 offset:692
	ds_read_b32 v38, v5 offset:824
	ds_read_b32 v39, v5 offset:956
	ds_read_b32 v40, v5 offset:1088
	ds_read_b32 v41, v5 offset:1220
	ds_read_b32 v42, v5 offset:1352
	ds_read_b32 v43, v5 offset:1484
	ds_read_b32 v44, v5 offset:1616
	ds_read_b32 v45, v5 offset:1748
	ds_read_b32 v46, v5 offset:1880
	ds_read_b32 v47, v5 offset:2012
	s_waitcnt lgkmcnt(0)
	v_mul_f32_e32 v16, s46, v16
	v_mul_f32_e32 v17, s46, v17
	v_mul_f32_e32 v18, s46, v18
	v_mul_f32_e32 v19, s46, v19
	v_mul_f32_e32 v20, s46, v20
	v_mul_f32_e32 v21, s46, v21
	v_mul_f32_e32 v22, s46, v22
	v_mul_f32_e32 v23, s46, v23
	v_mul_f32_e32 v24, s46, v24
	v_mul_f32_e32 v25, s46, v25
	v_mul_f32_e32 v26, s46, v26
	v_mul_f32_e32 v27, s46, v27
	v_mul_f32_e32 v28, s46, v28
	v_mul_f32_e32 v29, s46, v29
	v_mul_f32_e32 v30, s46, v30
	v_mul_f32_e32 v31, s46, v31
	v_mul_f32_e32 v32, s46, v32
	v_mul_f32_e32 v33, s46, v33
	v_mul_f32_e32 v34, s46, v34
	v_mul_f32_e32 v35, s46, v35
	v_mul_f32_e32 v36, s46, v36
	v_mul_f32_e32 v37, s46, v37
	v_mul_f32_e32 v38, s46, v38
	v_mul_f32_e32 v39, s46, v39
	v_mul_f32_e32 v40, s46, v40
	v_mul_f32_e32 v41, s46, v41
	v_mul_f32_e32 v42, s46, v42
	v_mul_f32_e32 v43, s46, v43
	v_mul_f32_e32 v44, s46, v44
	v_mul_f32_e32 v45, s46, v45
	v_mul_f32_e32 v46, s46, v46
	v_mul_f32_e32 v47, s46, v47
	v_cvt_pk_fp8_f32 v48, v16, v17
	v_cvt_pk_fp8_f32 v49, v20, v21
	v_cvt_pk_fp8_f32 v50, v24, v25
	v_cvt_pk_fp8_f32 v51, v28, v29
	v_cvt_pk_fp8_f32 v52, v32, v33
	v_cvt_pk_fp8_f32 v53, v36, v37
	v_cvt_pk_fp8_f32 v54, v40, v41
	v_cvt_pk_fp8_f32 v55, v44, v45
	v_cvt_pk_fp8_f32 v48, v18, v19 op_sel:[0,0,1]
	v_cvt_pk_fp8_f32 v49, v22, v23 op_sel:[0,0,1]
	v_cvt_pk_fp8_f32 v50, v26, v27 op_sel:[0,0,1]
	v_cvt_pk_fp8_f32 v51, v30, v31 op_sel:[0,0,1]
	v_cvt_pk_fp8_f32 v52, v34, v35 op_sel:[0,0,1]
	v_cvt_pk_fp8_f32 v53, v38, v39 op_sel:[0,0,1]
	v_cvt_pk_fp8_f32 v54, v42, v43 op_sel:[0,0,1]
	v_cvt_pk_fp8_f32 v55, v46, v47 op_sel:[0,0,1]
	ds_read_b32 v16, v5 offset:64
	ds_read_b32 v17, v5 offset:196
	ds_read_b32 v18, v5 offset:328
	ds_read_b32 v19, v5 offset:460
	ds_read_b32 v20, v5 offset:592
	ds_read_b32 v21, v5 offset:724
	ds_read_b32 v22, v5 offset:856
	ds_read_b32 v23, v5 offset:988
	ds_read_b32 v24, v5 offset:1120
	ds_read_b32 v25, v5 offset:1252
	ds_read_b32 v26, v5 offset:1384
	ds_read_b32 v27, v5 offset:1516
	ds_read_b32 v28, v5 offset:1648
	ds_read_b32 v29, v5 offset:1780
	ds_read_b32 v30, v5 offset:1912
	ds_read_b32 v31, v5 offset:2044
	ds_read_b32 v32, v5 offset:96
	ds_read_b32 v33, v5 offset:228
	ds_read_b32 v34, v5 offset:360
	ds_read_b32 v35, v5 offset:492
	ds_read_b32 v36, v5 offset:624
	ds_read_b32 v37, v5 offset:756
	ds_read_b32 v38, v5 offset:888
	ds_read_b32 v39, v5 offset:1020
	ds_read_b32 v40, v5 offset:1152
	ds_read_b32 v41, v5 offset:1284
	ds_read_b32 v42, v5 offset:1416
	ds_read_b32 v43, v5 offset:1548
	ds_read_b32 v44, v5 offset:1680
	ds_read_b32 v45, v5 offset:1812
	ds_read_b32 v46, v5 offset:1944
	ds_read_b32 v47, v5 offset:2076
	s_waitcnt lgkmcnt(0)
	v_mul_f32_e32 v16, s46, v16
	v_mul_f32_e32 v17, s46, v17
	v_mul_f32_e32 v18, s46, v18
	v_mul_f32_e32 v19, s46, v19
	v_mul_f32_e32 v20, s46, v20
	v_mul_f32_e32 v21, s46, v21
	v_mul_f32_e32 v22, s46, v22
	v_mul_f32_e32 v23, s46, v23
	v_mul_f32_e32 v24, s46, v24
	v_mul_f32_e32 v25, s46, v25
	v_mul_f32_e32 v26, s46, v26
	v_mul_f32_e32 v27, s46, v27
	v_mul_f32_e32 v28, s46, v28
	v_mul_f32_e32 v29, s46, v29
	v_mul_f32_e32 v30, s46, v30
	v_mul_f32_e32 v31, s46, v31
	v_mul_f32_e32 v32, s46, v32
	v_mul_f32_e32 v33, s46, v33
	v_mul_f32_e32 v34, s46, v34
	v_mul_f32_e32 v35, s46, v35
	v_mul_f32_e32 v36, s46, v36
	v_mul_f32_e32 v37, s46, v37
	v_mul_f32_e32 v38, s46, v38
	v_mul_f32_e32 v39, s46, v39
	v_mul_f32_e32 v40, s46, v40
	v_mul_f32_e32 v41, s46, v41
	v_mul_f32_e32 v42, s46, v42
	v_mul_f32_e32 v43, s46, v43
	v_mul_f32_e32 v44, s46, v44
	v_mul_f32_e32 v45, s46, v45
	v_mul_f32_e32 v46, s46, v46
	v_mul_f32_e32 v47, s46, v47
	v_cvt_pk_fp8_f32 v56, v16, v17
	v_cvt_pk_fp8_f32 v57, v20, v21
	v_cvt_pk_fp8_f32 v58, v24, v25
	v_cvt_pk_fp8_f32 v59, v28, v29
	v_cvt_pk_fp8_f32 v60, v32, v33
	v_cvt_pk_fp8_f32 v61, v36, v37
	v_cvt_pk_fp8_f32 v62, v40, v41
	v_cvt_pk_fp8_f32 v63, v44, v45
	v_cvt_pk_fp8_f32 v56, v18, v19 op_sel:[0,0,1]
	v_cvt_pk_fp8_f32 v57, v22, v23 op_sel:[0,0,1]
	v_cvt_pk_fp8_f32 v58, v26, v27 op_sel:[0,0,1]
	v_cvt_pk_fp8_f32 v59, v30, v31 op_sel:[0,0,1]
	v_cvt_pk_fp8_f32 v60, v34, v35 op_sel:[0,0,1]
	v_cvt_pk_fp8_f32 v61, v38, v39 op_sel:[0,0,1]
	v_cvt_pk_fp8_f32 v62, v42, v43 op_sel:[0,0,1]
	v_cvt_pk_fp8_f32 v63, v46, v47 op_sel:[0,0,1]
	s_nop 0
	global_store_dwordx4 v6, v[48:51], s[40:41]
	global_store_dwordx4 v7, v[52:55], s[40:41]
	global_store_dwordx4 v8, v[56:59], s[40:41]
	global_store_dwordx4 v9, v[60:63], s[40:41]
	s_cmp_lt_u32 s64, s65
	s_cbranch_scc1 .LcvE_loop
.LcvE_done:
	s_waitcnt vmcnt(0) lgkmcnt(0)
.LBB0_1091:
	s_mov_b64 s[14:15], 0

c_jobs:
	.long	4
	.long	2840
	.long	1024
	.long	0
	.long	1024
	.long	0
	.long	1
	.long	2
	.quad	2908160
	.quad	2097152
	.quad	2097152
	.long	0
	.long	0
	.long	4
	.long	2840
	.long	1024
	.long	1536
	.long	512
	.long	1024
	.long	1
	.long	2
	.quad	2908160
	.quad	2097152
	.quad	2097152
	.long	0
	.long	0
	.long	4
	.long	2840
	.long	1024
	.long	2048
	.long	128
	.long	1536
	.long	1
	.long	2
	.quad	2908160
	.quad	2097152
	.quad	2097152
	.long	0
	.long	0
	.long	4
	.long	2840
	.long	1024
	.long	2176
	.long	128
	.long	1664
	.long	1
	.long	2
	.quad	2908160
	.quad	2097152
	.quad	2097152
	.long	0
	.long	0
	.long	4
	.long	2840
	.long	1024
	.long	2304
	.long	128
	.long	1792
	.long	1
	.long	2
	.quad	2908160
	.quad	2097152
	.quad	2097152
	.long	0
	.long	0
	.long	4
	.long	2840
	.long	1024
	.long	2560
	.long	128
	.long	1920
	.long	1
	.long	2
	.quad	2908160
	.quad	2097152
	.quad	2097152
	.long	0
	.long	0
	.long	4
	.long	2840
	.long	1024
	.long	1024
	.long	512
	.long	0
	.long	0
	.long	2
	.quad	2908160
	.quad	10485760
	.quad	786432
	.long	0
	.long	0
	.long	4
	.long	2840
	.long	1024
	.long	2432
	.long	128
	.long	512
	.long	0
	.long	2
	.quad	2908160
	.quad	10485760
	.quad	786432
	.long	0
	.long	0
	.long	4
	.long	2840
	.long	1024
	.long	2688
	.long	128
	.long	640
	.long	0
	.long	2
	.quad	2908160
	.quad	10485760
	.quad	786432
	.long	0
	.long	0
	.long	5
	.long	1024
	.long	1024
	.long	0
	.long	1024
	.long	0
	.long	0
	.long	2
	.quad	1048576
	.quad	13631488
	.quad	1048576
	.long	64
	.long	0
	.long	13
	.long	256
	.long	2048
	.long	0
	.long	256
	.long	0
	.long	0
	.long	4
	.quad	524288
	.quad	17825792
	.quad	524288
	.long	0
	.long	0
	.long	15
	.long	6144
	.long	1024
	.long	0
	.long	2048
	.long	0
	.long	0
	.long	2
	.quad	6291456
	.quad	22020096
	.quad	4194304
	.long	32
	.long	0
	.long	15
	.long	6144
	.long	1024
	.long	4096
	.long	2048
	.long	2048
	.long	0
	.long	2
	.quad	6291456
	.quad	22020096
	.quad	4194304
	.long	32
	.long	0
	.long	15
	.long	6144
	.long	1024
	.long	2048
	.long	2048
	.long	0
	.long	0
	.long	2
	.quad	6291456
	.quad	38797312
	.quad	2097152
	.long	32
	.long	0
	.long	16
	.long	1024
	.long	2048
	.long	0
	.long	1024
	.long	0
	.long	0
	.long	2
	.quad	2097152
	.quad	51380224
	.quad	2097152
	.long	128
	.long	0
	.long	20
	.long	2048
	.long	1024
	.long	0
	.long	2048
	.long	0
	.long	2
	.long	104
	.quad	2097152
	.quad	71303168
	.quad	2097152
	.long	32
	.long	0
	.long	22
	.long	1024
	.long	1024
	.long	0
	.long	1024
	.long	0
	.long	0
	.long	104
	.quad	1048576
	.quad	608174080
	.quad	1048576
	.long	64
	.long	0
	.long	24
	.long	1024
	.long	256
	.long	0
	.long	1024
	.long	0
	.long	0
	.long	4
	.quad	262144
	.quad	59768832
	.quad	262144
	.long	0
	.long	0
	.long	25
	.long	1024
	.long	1024
	.long	0
	.long	1024
	.long	0
	.long	0
	.long	4
	.quad	1048576
	.quad	61865984
	.quad	1048576
	.long	32
	.long	0
	.size	c_jobs, 1216

	.type	__hip_cuid_b50e1a6430de2f85,@object
